# LN1 phase entry: first group's row loads issued before the gamma/beta wait + LDS staging + workgroup barrier
# speedup vs baseline: 1.0089x; 1.0021x over previous
.LBB0_3226:
	v_readlane_b32 s0, v253, 49
	v_mov_b32_e32 v66, v0
	v_readlane_b32 s14, v253, 0
	v_mov_b32_e32 v1, s0
	s_waitcnt vmcnt(0)
	ds_read2_b64 v[2:5], v1 offset1:1
	v_readlane_b32 s0, v253, 48
	s_waitcnt lgkmcnt(0)
	v_readfirstlane_b32 s2, v2
	v_mov_b32_e32 v1, s0
	v_readlane_b32 s0, v253, 50
	ds_read_b64 v[10:11], v1
	v_readfirstlane_b32 s3, v3
	v_mov_b32_e32 v1, s0
	v_readlane_b32 s0, v253, 51
	v_readfirstlane_b32 s5, v4
	v_readfirstlane_b32 s4, v5
	v_mov_b32_e32 v2, s0
	v_readlane_b32 s0, v253, 38
	s_waitcnt lgkmcnt(0)
	v_readfirstlane_b32 s6, v11
	v_readfirstlane_b32 s7, v10
	v_mov_b32_e32 v3, s0
	v_readlane_b32 s0, v254, 1
	s_lshl_b32 s64, s0, 12
	s_lshl_b64 s[0:1], s[64:65], 2
	s_add_u32 s2, s2, s0
	ds_read_b64 v[12:13], v1
	ds_read_b64 v[14:15], v2
	ds_read_b64 v[16:17], v3
	s_addc_u32 s3, s3, s1
	s_add_u32 s0, s5, s0
	v_ashrrev_i32_e32 v67, 31, v66
	v_lshlrev_b64 v[6:7], 4, v[66:67]
	s_addc_u32 s1, s4, s1
	v_lshl_add_u64 v[2:3], s[2:3], 0, v[6:7]
	global_load_dwordx4 v[180:183], v[2:3], off
	v_lshl_add_u64 v[6:7], s[0:1], 0, v[6:7]
	global_load_dwordx4 v[184:187], v[6:7], off
	v_lshl_add_u32 v1, v66, 4, 0
	v_readlane_b32 s0, v253, 5
	v_add_u32_e32 v188, 0x18000, v1
	v_readlane_b32 s1, v253, 6
	v_add_u32_e32 v189, 0x1a000, v1
	s_waitcnt lgkmcnt(2)
	v_readfirstlane_b32 s10, v13
	v_readfirstlane_b32 s12, v12
	s_waitcnt lgkmcnt(1)
	v_readfirstlane_b32 s11, v15
	v_readfirstlane_b32 s13, v14
	s_waitcnt lgkmcnt(0)
	v_readfirstlane_b32 s3, v17
	v_readfirstlane_b32 s2, v16
	v_readfirstlane_b32 s8, v66


	s_load_dword s36, s[0:1], 0x0
	s_waitcnt lgkmcnt(0)
	s_cmpk_gt_i32 s14, 0x1ff
	s_cbranch_scc1 .LBB0_3269
	s_add_u32 s9, s2, 0x6030000
	s_addc_u32 s15, s3, 0
	s_add_u32 s0, s2, 0xa030000
	s_addc_u32 s1, s3, 0
	s_add_u32 s4, s2, 0xe030000
	s_addc_u32 s5, s3, 0
	v_readlane_b32 s16, v254, 1
	s_cmp_eq_u32 s16, 0
	s_cselect_b32 s15, s6, s15
	s_cselect_b32 s16, s7, s9
	s_ashr_i32 s37, s8, 6
	s_lshl_b32 s17, s14, 4
	s_lshl_b32 s18, s37, 1
	s_add_i32 s6, s17, s18
	s_ashr_i32 s7, s6, 31
	s_lshl_b64 s[8:9], s[6:7], 12
	s_add_u32 s8, s4, s8
	v_and_b32_e32 v1, 63, v66
	s_addc_u32 s9, s5, s9
	s_lshl_b64 s[20:21], s[6:7], 13
	v_lshlrev_b32_e32 v70, 2, v1
	s_add_u32 s20, s16, s20
	s_addc_u32 s21, s15, s21
	v_or_b32_e32 v74, 0x400, v70
	v_or_b32_e32 v78, 0x500, v70
	v_or_b32_e32 v82, 0x600, v70
	v_or_b32_e32 v84, 0x700, v70
	s_or_b32 s6, s6, 1
	v_lshlrev_b32_e32 v68, 4, v1
	v_lshlrev_b32_e32 v106, 3, v1
	v_lshlrev_b32_e32 v86, 2, v74
	v_lshlrev_b32_e32 v104, 2, v78
	v_lshlrev_b32_e32 v105, 2, v82
	v_lshlrev_b32_e32 v118, 2, v84
	s_ashr_i32 s7, s6, 31
	global_load_dwordx4 v[2:5], v68, s[20:21] nt
	global_load_dwordx2 v[72:73], v106, s[8:9] nt
	global_load_dwordx4 v[6:9], v68, s[20:21] offset:1024 nt
	global_load_dwordx2 v[76:77], v106, s[8:9] offset:512 nt
	global_load_dwordx4 v[10:13], v68, s[20:21] offset:2048 nt
	global_load_dwordx2 v[80:81], v106, s[8:9] offset:1024 nt
	global_load_dwordx4 v[14:17], v68, s[20:21] offset:3072 nt
	global_load_dwordx2 v[88:89], v106, s[8:9] offset:1536 nt
	global_load_dwordx4 v[18:21], v86, s[20:21] nt
	global_load_dwordx2 v[90:91], v106, s[8:9] offset:2048 nt
	global_load_dwordx4 v[22:25], v104, s[20:21] nt
	global_load_dwordx2 v[92:93], v106, s[8:9] offset:2560 nt
	global_load_dwordx4 v[26:29], v105, s[20:21] nt
	global_load_dwordx2 v[94:95], v106, s[8:9] offset:3072 nt
	global_load_dwordx4 v[30:33], v118, s[20:21] nt
	global_load_dwordx2 v[96:97], v106, s[8:9] offset:3584 nt
	s_lshl_b64 s[8:9], s[6:7], 12
	s_add_u32 s8, s4, s8
	s_addc_u32 s9, s5, s9
	s_lshl_b64 s[6:7], s[6:7], 13
	s_add_u32 s6, s16, s6
	s_addc_u32 s7, s15, s7
	global_load_dwordx4 v[34:37], v68, s[6:7] nt
	global_load_dwordx2 v[98:99], v106, s[8:9] nt
	global_load_dwordx4 v[38:41], v68, s[6:7] offset:1024 nt
	global_load_dwordx2 v[100:101], v106, s[8:9] offset:512 nt
	global_load_dwordx4 v[42:45], v68, s[6:7] offset:2048 nt
	global_load_dwordx2 v[102:103], v106, s[8:9] offset:1024 nt
	global_load_dwordx4 v[46:49], v68, s[6:7] offset:3072 nt
	global_load_dwordx2 v[108:109], v106, s[8:9] offset:1536 nt
	global_load_dwordx4 v[50:53], v86, s[6:7] nt
	global_load_dwordx2 v[110:111], v106, s[8:9] offset:2048 nt
	global_load_dwordx4 v[54:57], v104, s[6:7] nt
	global_load_dwordx2 v[112:113], v106, s[8:9] offset:2560 nt
	global_load_dwordx4 v[58:61], v105, s[6:7] nt
	global_load_dwordx2 v[114:115], v106, s[8:9] offset:3072 nt
	global_load_dwordx4 v[62:65], v118, s[6:7] nt
	global_load_dwordx2 v[116:117], v106, s[8:9] offset:3584 nt
	s_waitcnt vmcnt(33)
	ds_write_b128 v188, v[180:183]
	s_waitcnt vmcnt(32)
	ds_write_b128 v189, v[184:187]
	s_waitcnt lgkmcnt(0)
	s_barrier
	v_and_b32_e32 v1, 64, v215
	v_add_u32_e32 v79, 64, v1
	v_xor_b32_e32 v1, 32, v215
	v_cmp_lt_i32_e32 vcc, v1, v79
	v_xor_b32_e32 v67, 16, v215
	v_xor_b32_e32 v69, 8, v215
	v_cndmask_b32_e32 v1, v215, v1, vcc
	v_cmp_lt_i32_e32 vcc, v67, v79
	v_xor_b32_e32 v71, 4, v215
	v_xor_b32_e32 v75, 2, v215
	v_cndmask_b32_e32 v67, v215, v67, vcc
	v_cmp_lt_i32_e32 vcc, v69, v79
	s_add_i32 s6, 0, 0x18000
	s_add_i32 s7, 0, 0x1a000
	v_cndmask_b32_e32 v69, v215, v69, vcc
	v_cmp_lt_i32_e32 vcc, v71, v79
	v_or_b32_e32 v119, 0x400, v68
	v_xor_b32_e32 v83, 1, v215
	v_cndmask_b32_e32 v71, v215, v71, vcc
	v_cmp_lt_i32_e32 vcc, v75, v79
	v_add_u32_e32 v150, s6, v119
	v_add_u32_e32 v151, s7, v119
	v_or_b32_e32 v119, 0x800, v68
	v_mov_b32_e32 v107, v87
	v_cndmask_b32_e32 v75, v215, v75, vcc
	v_cmp_lt_i32_e32 vcc, v83, v79
	v_add_u32_e32 v152, s6, v119
	v_add_u32_e32 v153, s7, v119
	v_or_b32_e32 v119, 0xc00, v68
	v_cndmask_b32_e32 v79, v215, v83, vcc
	v_add_u32_e32 v83, s6, v68
	v_add_u32_e32 v85, s7, v68
	v_add_u32_e32 v154, s6, v119
	v_add_u32_e32 v155, s7, v119
	v_add_u32_e32 v156, s6, v86
	v_add_u32_e32 v157, s7, v86
	v_add_u32_e32 v158, s6, v104
	v_add_u32_e32 v159, s7, v104
	v_add_u32_e32 v160, s6, v105
	v_add_u32_e32 v161, s7, v105
	v_add_u32_e32 v162, s6, v118
	v_add_u32_e32 v163, s7, v118
	v_lshl_add_u64 v[104:105], s[2:3], 0, v[106:107]
	s_mov_b64 s[6:7], 0x14030000
	v_lshl_add_u64 v[106:107], s[4:5], 0, v[106:107]
	s_add_i32 s4, s14, s36
	v_lshlrev_b32_e32 v1, 2, v1
	v_lshlrev_b32_e32 v67, 2, v67
	v_lshlrev_b32_e32 v69, 2, v69
	v_lshlrev_b32_e32 v71, 2, v71
	v_lshlrev_b32_e32 v75, 2, v75
	v_lshlrev_b32_e32 v79, 2, v79
	v_lshl_add_u64 v[104:105], v[104:105], 0, s[6:7]
	s_lshl_b32 s8, s36, 4
	s_lshl_b32 s9, s4, 4
	s_branch .LBB0_3229
